# k8 plus P11 on all 256 workgroups with each half-tile workgroup staging only the A half it uses (6 instead of 8 LDS-DMA pieces per K-tile)
# speedup vs baseline: 1.0097x; 1.0097x over previous
.LBB0_907:
	v_add_u32_e32 v166, s43, v131
	v_add_u32_e32 v182, s44, v131
	s_add_u32 s22, s8, s20
	ds_read_b128 v[154:157], v166
	ds_read_b128 v[158:161], v166 offset:1024
	ds_read_b128 v[162:165], v166 offset:2048
	ds_read_b128 v[166:169], v166 offset:3072
	ds_read_b128 v[170:173], v182
	ds_read_b128 v[174:177], v182 offset:1024
	ds_read_b128 v[178:181], v182 offset:2048
	ds_read_b128 v[182:185], v182 offset:3072
	s_addc_u32 s23, s9, s21
	s_add_u32 s22, s22, 0x100
	s_addc_u32 s23, s23, 0
	s_add_u32 s51, s46, s20
	s_addc_u32 s52, s47, s21
	s_cmpk_eq_i32 s20, 0xf00
	s_cselect_b32 s25, s15, s23
	s_cselect_b32 s24, s48, s22
	s_cselect_b32 s23, s13, s52
	s_cselect_b32 s22, s49, s51
	v_lshl_add_u64 v[218:219], v[150:151], 0, s[20:21]
	s_add_i32 m0, s7, 0xc000
	ds_read_b128 v[186:189], v133
	ds_read_b128 v[190:193], v133 offset:1024
	ds_read_b128 v[194:197], v133 offset:2048
	ds_read_b128 v[198:201], v133 offset:3072
	ds_read_b128 v[202:205], v133 offset:4096
	ds_read_b128 v[206:209], v133 offset:5120
	ds_read_b128 v[210:213], v133 offset:6144
	ds_read_b128 v[214:217], v133 offset:7168
	s_cmp_eq_u32 s100, 0
	s_cbranch_scc1 .Lp11_dma0
	global_load_lds_dwordx4 v[218:219], off
.Lp11_dma0:
	v_lshl_add_u64 v[218:219], v[152:153], 0, s[20:21]
	s_add_i32 m0, s7, 0xe000
	s_nop 0
	s_cmp_eq_u32 s100, 0
	s_cbranch_scc1 .Lp11_dma1
	global_load_lds_dwordx4 v[218:219], off
.Lp11_dma1:
	s_waitcnt vmcnt(6)
	s_waitcnt lgkmcnt(0)
	s_barrier
	s_setprio 1
	s_waitcnt lgkmcnt(0)
	s_cmp_eq_u32 s98, 0
	s_cbranch_scc1 .Lp11_skip0
	v_mfma_f32_16x16x32_bf16 v[126:129], v[154:157], v[186:189], v[126:129]
	v_mfma_f32_16x16x32_bf16 v[122:125], v[162:165], v[186:189], v[122:125]
	v_mfma_f32_16x16x32_bf16 v[114:117], v[154:157], v[194:197], v[114:117]
	v_mfma_f32_16x16x32_bf16 v[106:109], v[162:165], v[194:197], v[106:109]
	v_mfma_f32_16x16x32_bf16 v[98:101], v[154:157], v[202:205], v[98:101]
	v_mfma_f32_16x16x32_bf16 v[90:93], v[162:165], v[202:205], v[90:93]
	v_mfma_f32_16x16x32_bf16 v[82:85], v[154:157], v[210:213], v[82:85]
	v_mfma_f32_16x16x32_bf16 v[74:77], v[162:165], v[210:213], v[74:77]
	v_mfma_f32_16x16x32_bf16 v[126:129], v[158:161], v[190:193], v[126:129]
	v_mfma_f32_16x16x32_bf16 v[122:125], v[166:169], v[190:193], v[122:125]
	v_mfma_f32_16x16x32_bf16 v[114:117], v[158:161], v[198:201], v[114:117]
	v_mfma_f32_16x16x32_bf16 v[106:109], v[166:169], v[198:201], v[106:109]
	v_mfma_f32_16x16x32_bf16 v[98:101], v[158:161], v[206:209], v[98:101]
	v_mfma_f32_16x16x32_bf16 v[90:93], v[166:169], v[206:209], v[90:93]
	v_mfma_f32_16x16x32_bf16 v[82:85], v[158:161], v[214:217], v[82:85]
	v_mfma_f32_16x16x32_bf16 v[74:77], v[166:169], v[214:217], v[74:77]
	s_setprio 0
	s_setprio 1
	v_mfma_f32_16x16x32_bf16 v[118:121], v[170:173], v[186:189], v[118:121]
	v_mfma_f32_16x16x32_bf16 v[110:113], v[178:181], v[186:189], v[110:113]
	v_mfma_f32_16x16x32_bf16 v[102:105], v[170:173], v[194:197], v[102:105]
	v_mfma_f32_16x16x32_bf16 v[94:97], v[178:181], v[194:197], v[94:97]
	v_mfma_f32_16x16x32_bf16 v[86:89], v[170:173], v[202:205], v[86:89]
	v_mfma_f32_16x16x32_bf16 v[78:81], v[178:181], v[202:205], v[78:81]
	v_mfma_f32_16x16x32_bf16 v[70:73], v[170:173], v[210:213], v[70:73]
	v_mfma_f32_16x16x32_bf16 v[66:69], v[178:181], v[210:213], v[66:69]
	v_mfma_f32_16x16x32_bf16 v[118:121], v[174:177], v[190:193], v[118:121]
	v_mfma_f32_16x16x32_bf16 v[110:113], v[182:185], v[190:193], v[110:113]
	v_mfma_f32_16x16x32_bf16 v[102:105], v[174:177], v[198:201], v[102:105]
	v_mfma_f32_16x16x32_bf16 v[94:97], v[182:185], v[198:201], v[94:97]
	v_mfma_f32_16x16x32_bf16 v[86:89], v[174:177], v[206:209], v[86:89]
	v_mfma_f32_16x16x32_bf16 v[78:81], v[182:185], v[206:209], v[78:81]
	v_mfma_f32_16x16x32_bf16 v[70:73], v[174:177], v[214:217], v[70:73]
	v_mfma_f32_16x16x32_bf16 v[66:69], v[182:185], v[214:217], v[66:69]
.Lp11_skip0:
	s_setprio 0
	s_barrier
	s_add_i32 s51, s43, s36
	v_lshl_add_u64 v[218:219], s[22:23], 0, v[136:137]
	s_mov_b32 m0, s51
	ds_read_b128 v[186:189], v133 offset:16384
	ds_read_b128 v[190:193], v133 offset:17408
	ds_read_b128 v[194:197], v133 offset:18432
	ds_read_b128 v[198:201], v133 offset:19456
	ds_read_b128 v[202:205], v133 offset:20480
	ds_read_b128 v[206:209], v133 offset:21504
	ds_read_b128 v[210:213], v133 offset:22528
	ds_read_b128 v[214:217], v133 offset:23552
	global_load_lds_dwordx4 v[218:219], off
	s_add_i32 m0, s51, 0x2000
	s_add_u32 s52, s22, 0x80000
	v_lshl_add_u64 v[220:221], s[22:23], 0, v[140:141]
	s_addc_u32 s53, s23, 0
	s_add_i32 s51, s44, s36
	global_load_lds_dwordx4 v[220:221], off
	v_lshl_add_u64 v[222:223], s[52:53], 0, v[136:137]
	s_mov_b32 m0, s51
	v_lshl_add_u64 v[224:225], s[24:25], 0, v[138:139]
	global_load_lds_dwordx4 v[222:223], off
	v_lshl_add_u64 v[222:223], s[52:53], 0, v[140:141]
	s_add_i32 m0, s51, 0x2000
	s_nop 0
	global_load_lds_dwordx4 v[222:223], off
	v_lshl_add_u64 v[222:223], s[24:25], 0, v[134:135]
	s_mov_b32 m0, s7
	s_nop 0
	s_cmp_eq_u32 s98, 0
	s_cbranch_scc1 .Lp11_dma2
	global_load_lds_dwordx4 v[222:223], off
.Lp11_dma2:
	s_mov_b32 m0, s37
	s_nop 0
	s_cmp_eq_u32 s98, 0
	s_cbranch_scc1 .Lp11_dma3
	global_load_lds_dwordx4 v[224:225], off
.Lp11_dma3:
	s_waitcnt vmcnt(6)
	s_waitcnt lgkmcnt(0)
	s_barrier
	s_setprio 1
	s_waitcnt lgkmcnt(0)
	s_cmp_eq_u32 s100, 0
	s_cbranch_scc1 .Lp11_skip1
	v_mfma_f32_16x16x32_bf16 v[62:65], v[154:157], v[186:189], v[62:65]
	v_mfma_f32_16x16x32_bf16 v[58:61], v[162:165], v[186:189], v[58:61]
	v_mfma_f32_16x16x32_bf16 v[50:53], v[154:157], v[194:197], v[50:53]
	v_mfma_f32_16x16x32_bf16 v[42:45], v[162:165], v[194:197], v[42:45]
	v_mfma_f32_16x16x32_bf16 v[34:37], v[154:157], v[202:205], v[34:37]
	v_mfma_f32_16x16x32_bf16 v[26:29], v[162:165], v[202:205], v[26:29]
	v_mfma_f32_16x16x32_bf16 v[18:21], v[154:157], v[210:213], v[18:21]
	v_mfma_f32_16x16x32_bf16 v[10:13], v[162:165], v[210:213], v[10:13]
	v_mfma_f32_16x16x32_bf16 v[62:65], v[158:161], v[190:193], v[62:65]
	v_mfma_f32_16x16x32_bf16 v[58:61], v[166:169], v[190:193], v[58:61]
	v_mfma_f32_16x16x32_bf16 v[50:53], v[158:161], v[198:201], v[50:53]
	v_mfma_f32_16x16x32_bf16 v[42:45], v[166:169], v[198:201], v[42:45]
	v_mfma_f32_16x16x32_bf16 v[34:37], v[158:161], v[206:209], v[34:37]
	v_mfma_f32_16x16x32_bf16 v[26:29], v[166:169], v[206:209], v[26:29]
	v_mfma_f32_16x16x32_bf16 v[18:21], v[158:161], v[214:217], v[18:21]
	v_mfma_f32_16x16x32_bf16 v[10:13], v[166:169], v[214:217], v[10:13]
	s_setprio 0
	s_setprio 1
	v_mfma_f32_16x16x32_bf16 v[54:57], v[170:173], v[186:189], v[54:57]
	v_mfma_f32_16x16x32_bf16 v[46:49], v[178:181], v[186:189], v[46:49]
	v_mfma_f32_16x16x32_bf16 v[38:41], v[170:173], v[194:197], v[38:41]
	v_mfma_f32_16x16x32_bf16 v[30:33], v[178:181], v[194:197], v[30:33]
	v_mfma_f32_16x16x32_bf16 v[22:25], v[170:173], v[202:205], v[22:25]
	v_mfma_f32_16x16x32_bf16 v[14:17], v[178:181], v[202:205], v[14:17]
	v_mfma_f32_16x16x32_bf16 v[6:9], v[170:173], v[210:213], v[6:9]
	v_mfma_f32_16x16x32_bf16 v[2:5], v[178:181], v[210:213], v[2:5]
	v_mfma_f32_16x16x32_bf16 v[54:57], v[174:177], v[190:193], v[54:57]
	v_mfma_f32_16x16x32_bf16 v[46:49], v[182:185], v[190:193], v[46:49]
	v_mfma_f32_16x16x32_bf16 v[38:41], v[174:177], v[198:201], v[38:41]
	v_mfma_f32_16x16x32_bf16 v[30:33], v[182:185], v[198:201], v[30:33]
	v_mfma_f32_16x16x32_bf16 v[22:25], v[174:177], v[206:209], v[22:25]
	v_mfma_f32_16x16x32_bf16 v[14:17], v[182:185], v[206:209], v[14:17]
	v_mfma_f32_16x16x32_bf16 v[6:9], v[174:177], v[214:217], v[6:9]
	v_mfma_f32_16x16x32_bf16 v[2:5], v[182:185], v[214:217], v[2:5]
.Lp11_skip1:
	s_setprio 0
	s_barrier
	s_add_i32 s51, 0, 0x18000
	s_add_i32 s52, 0, 0x1c000
	v_add_u32_e32 v166, s51, v131
	v_add_u32_e32 v182, s52, v131
	ds_read_b128 v[154:157], v166
	ds_read_b128 v[158:161], v166 offset:1024
	ds_read_b128 v[162:165], v166 offset:2048
	ds_read_b128 v[166:169], v166 offset:3072
	ds_read_b128 v[170:173], v182
	ds_read_b128 v[174:177], v182 offset:1024
	ds_read_b128 v[178:181], v182 offset:2048
	ds_read_b128 v[182:185], v182 offset:3072
	s_add_u32 s24, s24, 0x80000
	s_addc_u32 s25, s25, 0
	s_mov_b32 m0, s38
	v_lshl_add_u64 v[226:227], s[24:25], 0, v[134:135]
	ds_read_b128 v[186:189], v133 offset:32768
	ds_read_b128 v[190:193], v133 offset:33792
	ds_read_b128 v[194:197], v133 offset:34816
	ds_read_b128 v[198:201], v133 offset:35840
	ds_read_b128 v[202:205], v133 offset:36864
	ds_read_b128 v[206:209], v133 offset:37888
	ds_read_b128 v[210:213], v133 offset:38912
	ds_read_b128 v[214:217], v133 offset:39936
	s_cmp_eq_u32 s100, 0
	s_cbranch_scc1 .Lp11_dma4
	global_load_lds_dwordx4 v[226:227], off
.Lp11_dma4:
	v_lshl_add_u64 v[226:227], s[24:25], 0, v[138:139]
	s_mov_b32 m0, s39
	s_nop 0
	s_cmp_eq_u32 s100, 0
	s_cbranch_scc1 .Lp11_dma5
	global_load_lds_dwordx4 v[226:227], off

.Lp11_skip2:
	s_setprio 0
	s_barrier
	s_add_i32 s24, s51, s36
	v_lshl_add_u64 v[218:219], v[218:219], 0, s[10:11]
	s_mov_b32 m0, s24
	ds_read_b128 v[186:189], v133 offset:49152
	ds_read_b128 v[190:193], v133 offset:50176
	ds_read_b128 v[194:197], v133 offset:51200
	ds_read_b128 v[198:201], v133 offset:52224
	ds_read_b128 v[202:205], v133 offset:53248
	ds_read_b128 v[206:209], v133 offset:54272
	ds_read_b128 v[210:213], v133 offset:55296
	ds_read_b128 v[214:217], v133 offset:56320
	global_load_lds_dwordx4 v[218:219], off
	s_add_i32 m0, s24, 0x2000
	s_add_u32 s22, s22, 0x80080
	v_lshl_add_u64 v[218:219], v[220:221], 0, s[10:11]
	s_addc_u32 s23, s23, 0
	s_add_i32 s24, s52, s36
	global_load_lds_dwordx4 v[218:219], off
	v_lshl_add_u64 v[218:219], s[22:23], 0, v[136:137]
	s_mov_b32 m0, s24
	s_nop 0
	global_load_lds_dwordx4 v[218:219], off
	v_lshl_add_u64 v[218:219], s[22:23], 0, v[140:141]
	s_add_i32 m0, s24, 0x2000
	s_nop 0
	global_load_lds_dwordx4 v[218:219], off
	v_lshl_add_u64 v[218:219], v[222:223], 0, s[10:11]
	s_mov_b32 m0, s40
	s_nop 0
	s_cmp_eq_u32 s98, 0
	s_cbranch_scc1 .Lp11_dma6
	global_load_lds_dwordx4 v[218:219], off
.Lp11_dma6:
	v_lshl_add_u64 v[218:219], v[224:225], 0, s[10:11]
	s_mov_b32 m0, s41
	s_nop 0
	s_cmp_eq_u32 s98, 0
	s_cbranch_scc1 .Lp11_dma7
	global_load_lds_dwordx4 v[218:219], off
